# speedup vs baseline: 1.0508x; 1.0234x over previous
_Z11main_kernelPKcPfS1_:
	s_load_dwordx2 s[6:7], s[0:1], 0x0
	s_and_b32 s3, s2, 7
	s_lshr_b32 s4, s2, 3
	s_and_b32 s5, s4, 3
	s_lshl_b32 s3, s3, 2
	s_or_b32 s8, s3, s5
	s_lshr_b32 s9, s4, 2
	v_lshrrev_b32_e32 v127, 6, v0
	v_and_b32_e32 v124, 63, v0
	v_lshlrev_b32_e32 v124, 4, v124
	v_mov_b32_e32 v120, 0
	v_readfirstlane_b32 s12, v127
	v_mov_b32_e32 v121, 0
	v_mov_b32_e32 v122, 0
	v_mov_b32_e32 v123, 0
	s_lshl_b32 s13, s12, 10
	s_lshl_b32 s14, s9, 3
	s_add_u32 s14, s14, s12
	s_lshl_b32 s15, s14, 13
	s_mul_i32 s16, s8, 0x18000
	s_add_u32 s16, s16, 0x100000
	v_or_b32_e32 v125, s13, v124
	v_or_b32_e32 v126, 0x2000, v125
	s_add_u32 s20, s13, 0x2000
	s_waitcnt lgkmcnt(0)
	s_add_u32 s10, s6, s16
	s_addc_u32 s11, s7, 0
	s_add_u32 s18, s6, s15
	s_addc_u32 s19, s7, 0
	s_add_u32 s22, s18, 0x1000
	s_addc_u32 s23, s19, 0
	s_mov_b32 m0, s13
	s_nop 0
	global_load_lds_dwordx4 v125, s[10:11]
	s_mov_b32 m0, s20
	s_nop 0
	global_load_lds_dwordx4 v126, s[10:11]
	global_load_dwordx4 v[96:99], v124, s[18:19]
	global_load_dwordx2 v[100:101], v124, s[18:19] offset:1024
	global_load_dwordx4 v[102:105], v124, s[18:19] offset:2048
	global_load_dwordx2 v[106:107], v124, s[18:19] offset:3072
	global_load_dwordx4 v[108:111], v124, s[22:23]
	global_load_dwordx2 v[112:113], v124, s[22:23] offset:1024
	global_load_dwordx4 v[114:117], v124, s[22:23] offset:2048
	global_load_dwordx2 v[118:119], v124, s[22:23] offset:3072
	s_add_u32 s24, s10, 0x4000
	s_addc_u32 s25, s11, 0
	s_add_u32 s26, s13, 0x4000
	s_mov_b32 m0, s26
	s_nop 0
	global_load_lds_dwordx4 v125, s[24:25]
	s_add_u32 s26, s20, 0x4000
	s_mov_b32 m0, s26
	s_nop 0
	global_load_lds_dwordx4 v126, s[24:25]
	s_add_u32 s24, s10, 0x8000
	s_addc_u32 s25, s11, 0
	s_add_u32 s26, s13, 0x8000
	s_mov_b32 m0, s26
	s_nop 0
	global_load_lds_dwordx4 v125, s[24:25]
	s_add_u32 s26, s20, 0x8000
	s_mov_b32 m0, s26
	s_nop 0
	global_load_lds_dwordx4 v126, s[24:25]
	s_add_u32 s24, s10, 0xc000
	s_addc_u32 s25, s11, 0
	s_add_u32 s26, s13, 0xc000
	s_mov_b32 m0, s26
	s_nop 0
	global_load_lds_dwordx4 v125, s[24:25]
	s_add_u32 s26, s20, 0xc000
	s_mov_b32 m0, s26
	s_nop 0
	global_load_lds_dwordx4 v126, s[24:25]
	s_waitcnt vmcnt(6)
	s_barrier
	ds_read_b128 v[0:3], v124
	ds_read_b64 v[4:5], v124 offset:1024
	ds_read_b128 v[6:9], v124 offset:2048
	ds_read_b64 v[10:11], v124 offset:3072
	ds_read_b128 v[12:15], v124 offset:4096
	ds_read_b64 v[16:17], v124 offset:5120
	ds_read_b128 v[18:21], v124 offset:6144
	ds_read_b64 v[22:23], v124 offset:7168
	s_waitcnt lgkmcnt(0)
	s_setprio 3
	v_mfma_f32_32x32x64_f8f6f4 v[48:63], v[0:5], v[96:101], 0 cbsz:2 blgp:2
	ds_read_b128 v[24:27], v124 offset:8192
	ds_read_b64 v[28:29], v124 offset:9216
	v_mfma_f32_32x32x64_f8f6f4 v[48:63], v[6:11], v[102:107], v[48:63] cbsz:2 blgp:2
	ds_read_b128 v[30:33], v124 offset:10240
	ds_read_b64 v[34:35], v124 offset:11264
	v_mfma_f32_32x32x64_f8f6f4 v[48:63], v[12:17], v[108:113], v[48:63] cbsz:2 blgp:2
	ds_read_b128 v[36:39], v124 offset:12288
	ds_read_b64 v[40:41], v124 offset:13312
	v_mfma_f32_32x32x64_f8f6f4 v[48:63], v[18:23], v[114:119], v[48:63] cbsz:2 blgp:2
	ds_read_b128 v[42:45], v124 offset:14336
	ds_read_b64 v[46:47], v124 offset:15360
	s_waitcnt vmcnt(4) lgkmcnt(0)
	s_barrier
	s_add_u32 s24, s10, 0x10000
	s_addc_u32 s25, s11, 0
	s_mov_b32 m0, s13
	s_nop 0
	global_load_lds_dwordx4 v125, s[24:25]
	s_mov_b32 m0, s20
	s_nop 0
	global_load_lds_dwordx4 v126, s[24:25]
	v_mfma_f32_32x32x64_f8f6f4 v[64:79], v[24:29], v[96:101], 0 cbsz:2 blgp:2
	ds_read_b128 v[0:3], v124 offset:16384
	ds_read_b64 v[4:5], v124 offset:17408
	ds_read_b128 v[6:9], v124 offset:18432
	ds_read_b64 v[10:11], v124 offset:19456
	ds_read_b128 v[24:27], v124 offset:24576
	ds_read_b64 v[28:29], v124 offset:25600
	v_mfma_f32_32x32x64_f8f6f4 v[64:79], v[30:35], v[102:107], v[64:79] cbsz:2 blgp:2
	ds_read_b128 v[12:15], v124 offset:20480
	ds_read_b64 v[16:17], v124 offset:21504
	ds_read_b128 v[18:21], v124 offset:22528
	ds_read_b64 v[22:23], v124 offset:23552
	ds_read_b128 v[30:33], v124 offset:26624
	ds_read_b64 v[34:35], v124 offset:27648
	v_exp_f32_e32 v48, v48
	v_exp_f32_e32 v49, v49
	v_exp_f32_e32 v50, v50
	v_exp_f32_e32 v51, v51
	v_pk_add_f32 v[120:121], v[120:121], v[48:49]
	v_pk_add_f32 v[122:123], v[122:123], v[50:51]
	v_mfma_f32_32x32x64_f8f6f4 v[64:79], v[36:41], v[108:113], v[64:79] cbsz:2 blgp:2
	ds_read_b128 v[36:39], v124 offset:28672
	ds_read_b64 v[40:41], v124 offset:29696
	v_exp_f32_e32 v52, v52
	v_exp_f32_e32 v53, v53
	v_exp_f32_e32 v54, v54
	v_exp_f32_e32 v55, v55
	v_pk_add_f32 v[120:121], v[120:121], v[52:53]
	v_pk_add_f32 v[122:123], v[122:123], v[54:55]
	v_mfma_f32_32x32x64_f8f6f4 v[64:79], v[42:47], v[114:119], v[64:79] cbsz:2 blgp:2
	ds_read_b128 v[42:45], v124 offset:30720
	ds_read_b64 v[46:47], v124 offset:31744
	v_exp_f32_e32 v56, v56
	v_exp_f32_e32 v57, v57
	v_exp_f32_e32 v58, v58
	v_exp_f32_e32 v59, v59
	v_pk_add_f32 v[120:121], v[120:121], v[56:57]
	v_pk_add_f32 v[122:123], v[122:123], v[58:59]
	s_waitcnt vmcnt(4) lgkmcnt(6)
	s_barrier
	v_mfma_f32_32x32x64_f8f6f4 v[80:95], v[0:5], v[96:101], 0 cbsz:2 blgp:2
	ds_read_b128 v[0:3], v124 offset:32768
	ds_read_b64 v[4:5], v124 offset:33792
	v_exp_f32_e32 v60, v60
	v_exp_f32_e32 v61, v61
	v_exp_f32_e32 v62, v62
	v_exp_f32_e32 v63, v63
	v_pk_add_f32 v[120:121], v[120:121], v[60:61]
	v_pk_add_f32 v[122:123], v[122:123], v[62:63]
	v_mfma_f32_32x32x64_f8f6f4 v[80:95], v[6:11], v[102:107], v[80:95] cbsz:2 blgp:2
	ds_read_b128 v[6:9], v124 offset:34816
	ds_read_b64 v[10:11], v124 offset:35840
	v_exp_f32_e32 v64, v64
	v_exp_f32_e32 v65, v65
	v_exp_f32_e32 v66, v66
	v_exp_f32_e32 v67, v67
	v_pk_add_f32 v[120:121], v[120:121], v[64:65]
	v_pk_add_f32 v[122:123], v[122:123], v[66:67]
	v_mfma_f32_32x32x64_f8f6f4 v[80:95], v[12:17], v[108:113], v[80:95] cbsz:2 blgp:2
	ds_read_b128 v[12:15], v124 offset:36864
	ds_read_b64 v[16:17], v124 offset:37888
	v_exp_f32_e32 v68, v68
	v_exp_f32_e32 v69, v69
	v_exp_f32_e32 v70, v70
	v_exp_f32_e32 v71, v71
	v_pk_add_f32 v[120:121], v[120:121], v[68:69]
	v_pk_add_f32 v[122:123], v[122:123], v[70:71]
	v_mfma_f32_32x32x64_f8f6f4 v[80:95], v[18:23], v[114:119], v[80:95] cbsz:2 blgp:2
	ds_read_b128 v[18:21], v124 offset:38912
	ds_read_b64 v[22:23], v124 offset:39936
	v_exp_f32_e32 v72, v72
	v_exp_f32_e32 v73, v73
	v_exp_f32_e32 v74, v74
	v_exp_f32_e32 v75, v75
	v_pk_add_f32 v[120:121], v[120:121], v[72:73]
	v_pk_add_f32 v[122:123], v[122:123], v[74:75]
	s_waitcnt lgkmcnt(8)
	v_mfma_f32_32x32x64_f8f6f4 v[48:63], v[24:29], v[96:101], 0 cbsz:2 blgp:2
	ds_read_b128 v[24:27], v124 offset:40960
	ds_read_b64 v[28:29], v124 offset:41984
	v_exp_f32_e32 v76, v76
	v_exp_f32_e32 v77, v77
	v_exp_f32_e32 v78, v78
	v_exp_f32_e32 v79, v79
	v_pk_add_f32 v[120:121], v[120:121], v[76:77]
	v_pk_add_f32 v[122:123], v[122:123], v[78:79]
	v_mfma_f32_32x32x64_f8f6f4 v[48:63], v[30:35], v[102:107], v[48:63] cbsz:2 blgp:2
	ds_read_b128 v[30:33], v124 offset:43008
	ds_read_b64 v[34:35], v124 offset:44032
	v_exp_f32_e32 v80, v80
	v_exp_f32_e32 v81, v81
	v_exp_f32_e32 v82, v82
	v_exp_f32_e32 v83, v83
	v_pk_add_f32 v[120:121], v[120:121], v[80:81]
	v_pk_add_f32 v[122:123], v[122:123], v[82:83]
	v_mfma_f32_32x32x64_f8f6f4 v[48:63], v[36:41], v[108:113], v[48:63] cbsz:2 blgp:2
	ds_read_b128 v[36:39], v124 offset:45056
	ds_read_b64 v[40:41], v124 offset:46080
	v_exp_f32_e32 v84, v84
	v_exp_f32_e32 v85, v85
	v_exp_f32_e32 v86, v86
	v_exp_f32_e32 v87, v87
	v_pk_add_f32 v[120:121], v[120:121], v[84:85]
	v_pk_add_f32 v[122:123], v[122:123], v[86:87]
	v_mfma_f32_32x32x64_f8f6f4 v[48:63], v[42:47], v[114:119], v[48:63] cbsz:2 blgp:2
	ds_read_b128 v[42:45], v124 offset:47104
	ds_read_b64 v[46:47], v124 offset:48128
	v_exp_f32_e32 v88, v88
	v_exp_f32_e32 v89, v89
	v_exp_f32_e32 v90, v90
	v_exp_f32_e32 v91, v91
	v_pk_add_f32 v[120:121], v[120:121], v[88:89]
	v_pk_add_f32 v[122:123], v[122:123], v[90:91]
	s_setprio 2
	s_waitcnt vmcnt(2) lgkmcnt(8)
	s_barrier
	s_add_u32 s24, s10, 0x14000
	s_addc_u32 s25, s11, 0
	s_add_u32 s26, s13, 0x4000
	s_mov_b32 m0, s26
	s_nop 0
	global_load_lds_dwordx4 v125, s[24:25]
	s_add_u32 s26, s20, 0x4000
	s_mov_b32 m0, s26
	s_nop 0
	global_load_lds_dwordx4 v126, s[24:25]
	v_mfma_f32_32x32x64_f8f6f4 v[64:79], v[0:5], v[96:101], 0 cbsz:2 blgp:2
	ds_read_b128 v[0:3], v124 offset:49152
	ds_read_b64 v[4:5], v124 offset:50176
	v_exp_f32_e32 v92, v92
	v_exp_f32_e32 v93, v93
	v_exp_f32_e32 v94, v94
	v_exp_f32_e32 v95, v95
	v_pk_add_f32 v[120:121], v[120:121], v[92:93]
	v_pk_add_f32 v[122:123], v[122:123], v[94:95]
	v_mfma_f32_32x32x64_f8f6f4 v[64:79], v[6:11], v[102:107], v[64:79] cbsz:2 blgp:2
	ds_read_b128 v[6:9], v124 offset:51200
	ds_read_b64 v[10:11], v124 offset:52224
	v_exp_f32_e32 v48, v48
	v_exp_f32_e32 v49, v49
	v_exp_f32_e32 v50, v50
	v_exp_f32_e32 v51, v51
	v_pk_add_f32 v[120:121], v[120:121], v[48:49]
	v_pk_add_f32 v[122:123], v[122:123], v[50:51]
	v_mfma_f32_32x32x64_f8f6f4 v[64:79], v[12:17], v[108:113], v[64:79] cbsz:2 blgp:2
	ds_read_b128 v[12:15], v124 offset:53248
	ds_read_b64 v[16:17], v124 offset:54272
	v_exp_f32_e32 v52, v52
	v_exp_f32_e32 v53, v53
	v_exp_f32_e32 v54, v54
	v_exp_f32_e32 v55, v55
	v_pk_add_f32 v[120:121], v[120:121], v[52:53]
	v_pk_add_f32 v[122:123], v[122:123], v[54:55]
	v_mfma_f32_32x32x64_f8f6f4 v[64:79], v[18:23], v[114:119], v[64:79] cbsz:2 blgp:2
	ds_read_b128 v[18:21], v124 offset:55296
	ds_read_b64 v[22:23], v124 offset:56320
	v_exp_f32_e32 v56, v56
	v_exp_f32_e32 v57, v57
	v_exp_f32_e32 v58, v58
	v_exp_f32_e32 v59, v59
	v_pk_add_f32 v[120:121], v[120:121], v[56:57]
	v_pk_add_f32 v[122:123], v[122:123], v[58:59]
	s_waitcnt lgkmcnt(8)
	v_mfma_f32_32x32x64_f8f6f4 v[80:95], v[24:29], v[96:101], 0 cbsz:2 blgp:2
	ds_read_b128 v[24:27], v124 offset:57344
	ds_read_b64 v[28:29], v124 offset:58368
	v_exp_f32_e32 v60, v60
	v_exp_f32_e32 v61, v61
	v_exp_f32_e32 v62, v62
	v_exp_f32_e32 v63, v63
	v_pk_add_f32 v[120:121], v[120:121], v[60:61]
	v_pk_add_f32 v[122:123], v[122:123], v[62:63]
	v_mfma_f32_32x32x64_f8f6f4 v[80:95], v[30:35], v[102:107], v[80:95] cbsz:2 blgp:2
	ds_read_b128 v[30:33], v124 offset:59392
	ds_read_b64 v[34:35], v124 offset:60416
	v_exp_f32_e32 v64, v64
	v_exp_f32_e32 v65, v65
	v_exp_f32_e32 v66, v66
	v_exp_f32_e32 v67, v67
	v_pk_add_f32 v[120:121], v[120:121], v[64:65]
	v_pk_add_f32 v[122:123], v[122:123], v[66:67]
	v_mfma_f32_32x32x64_f8f6f4 v[80:95], v[36:41], v[108:113], v[80:95] cbsz:2 blgp:2
	ds_read_b128 v[36:39], v124 offset:61440
	ds_read_b64 v[40:41], v124 offset:62464
	v_exp_f32_e32 v68, v68
	v_exp_f32_e32 v69, v69
	v_exp_f32_e32 v70, v70
	v_exp_f32_e32 v71, v71
	v_pk_add_f32 v[120:121], v[120:121], v[68:69]
	v_pk_add_f32 v[122:123], v[122:123], v[70:71]
	v_mfma_f32_32x32x64_f8f6f4 v[80:95], v[42:47], v[114:119], v[80:95] cbsz:2 blgp:2
	ds_read_b128 v[42:45], v124 offset:63488
	ds_read_b64 v[46:47], v124 offset:64512
	v_exp_f32_e32 v72, v72
	v_exp_f32_e32 v73, v73
	v_exp_f32_e32 v74, v74
	v_exp_f32_e32 v75, v75
	v_pk_add_f32 v[120:121], v[120:121], v[72:73]
	v_pk_add_f32 v[122:123], v[122:123], v[74:75]
	s_waitcnt vmcnt(2) lgkmcnt(8)
	s_barrier
	v_mfma_f32_32x32x64_f8f6f4 v[48:63], v[0:5], v[96:101], 0 cbsz:2 blgp:2
	ds_read_b128 v[0:3], v124
	ds_read_b64 v[4:5], v124 offset:1024
	v_exp_f32_e32 v76, v76
	v_exp_f32_e32 v77, v77
	v_exp_f32_e32 v78, v78
	v_exp_f32_e32 v79, v79
	v_pk_add_f32 v[120:121], v[120:121], v[76:77]
	v_pk_add_f32 v[122:123], v[122:123], v[78:79]
	v_mfma_f32_32x32x64_f8f6f4 v[48:63], v[6:11], v[102:107], v[48:63] cbsz:2 blgp:2
	ds_read_b128 v[6:9], v124 offset:2048
	ds_read_b64 v[10:11], v124 offset:3072
	v_exp_f32_e32 v80, v80
	v_exp_f32_e32 v81, v81
	v_exp_f32_e32 v82, v82
	v_exp_f32_e32 v83, v83
	v_pk_add_f32 v[120:121], v[120:121], v[80:81]
	v_pk_add_f32 v[122:123], v[122:123], v[82:83]
	v_mfma_f32_32x32x64_f8f6f4 v[48:63], v[12:17], v[108:113], v[48:63] cbsz:2 blgp:2
	ds_read_b128 v[12:15], v124 offset:4096
	ds_read_b64 v[16:17], v124 offset:5120
	v_exp_f32_e32 v84, v84
	v_exp_f32_e32 v85, v85
	v_exp_f32_e32 v86, v86
	v_exp_f32_e32 v87, v87
	v_pk_add_f32 v[120:121], v[120:121], v[84:85]
	v_pk_add_f32 v[122:123], v[122:123], v[86:87]
	v_mfma_f32_32x32x64_f8f6f4 v[48:63], v[18:23], v[114:119], v[48:63] cbsz:2 blgp:2
	ds_read_b128 v[18:21], v124 offset:6144
	ds_read_b64 v[22:23], v124 offset:7168
	v_exp_f32_e32 v88, v88
	v_exp_f32_e32 v89, v89
	v_exp_f32_e32 v90, v90
	v_exp_f32_e32 v91, v91
	v_pk_add_f32 v[120:121], v[120:121], v[88:89]
	v_pk_add_f32 v[122:123], v[122:123], v[90:91]
	s_waitcnt lgkmcnt(8)
	v_mfma_f32_32x32x64_f8f6f4 v[64:79], v[24:29], v[96:101], 0 cbsz:2 blgp:2
	ds_read_b128 v[24:27], v124 offset:8192
	ds_read_b64 v[28:29], v124 offset:9216
	v_exp_f32_e32 v92, v92
	v_exp_f32_e32 v93, v93
	v_exp_f32_e32 v94, v94
	v_exp_f32_e32 v95, v95
	v_pk_add_f32 v[120:121], v[120:121], v[92:93]
	v_pk_add_f32 v[122:123], v[122:123], v[94:95]
	v_mfma_f32_32x32x64_f8f6f4 v[64:79], v[30:35], v[102:107], v[64:79] cbsz:2 blgp:2
	ds_read_b128 v[30:33], v124 offset:10240
	ds_read_b64 v[34:35], v124 offset:11264
	v_exp_f32_e32 v48, v48
	v_exp_f32_e32 v49, v49
	v_exp_f32_e32 v50, v50
	v_exp_f32_e32 v51, v51
	v_pk_add_f32 v[120:121], v[120:121], v[48:49]
	v_pk_add_f32 v[122:123], v[122:123], v[50:51]
	v_mfma_f32_32x32x64_f8f6f4 v[64:79], v[36:41], v[108:113], v[64:79] cbsz:2 blgp:2
	ds_read_b128 v[36:39], v124 offset:12288
	ds_read_b64 v[40:41], v124 offset:13312
	v_exp_f32_e32 v52, v52
	v_exp_f32_e32 v53, v53
	v_exp_f32_e32 v54, v54
	v_exp_f32_e32 v55, v55
	v_pk_add_f32 v[120:121], v[120:121], v[52:53]
	v_pk_add_f32 v[122:123], v[122:123], v[54:55]
	v_mfma_f32_32x32x64_f8f6f4 v[64:79], v[42:47], v[114:119], v[64:79] cbsz:2 blgp:2
	ds_read_b128 v[42:45], v124 offset:14336
	ds_read_b64 v[46:47], v124 offset:15360
	v_exp_f32_e32 v56, v56
	v_exp_f32_e32 v57, v57
	v_exp_f32_e32 v58, v58
	v_exp_f32_e32 v59, v59
	v_pk_add_f32 v[120:121], v[120:121], v[56:57]
	v_pk_add_f32 v[122:123], v[122:123], v[58:59]
	s_setprio 1
	s_waitcnt vmcnt(0) lgkmcnt(8)
	s_barrier
	v_mfma_f32_32x32x64_f8f6f4 v[80:95], v[0:5], v[96:101], 0 cbsz:2 blgp:2
	ds_read_b128 v[0:3], v124 offset:16384
	ds_read_b64 v[4:5], v124 offset:17408
	v_exp_f32_e32 v60, v60
	v_exp_f32_e32 v61, v61
	v_exp_f32_e32 v62, v62
	v_exp_f32_e32 v63, v63
	v_pk_add_f32 v[120:121], v[120:121], v[60:61]
	v_pk_add_f32 v[122:123], v[122:123], v[62:63]
	v_mfma_f32_32x32x64_f8f6f4 v[80:95], v[6:11], v[102:107], v[80:95] cbsz:2 blgp:2
	ds_read_b128 v[6:9], v124 offset:18432
	ds_read_b64 v[10:11], v124 offset:19456
	v_exp_f32_e32 v64, v64
	v_exp_f32_e32 v65, v65
	v_exp_f32_e32 v66, v66
	v_exp_f32_e32 v67, v67
	v_pk_add_f32 v[120:121], v[120:121], v[64:65]
	v_pk_add_f32 v[122:123], v[122:123], v[66:67]
	v_mfma_f32_32x32x64_f8f6f4 v[80:95], v[12:17], v[108:113], v[80:95] cbsz:2 blgp:2
	ds_read_b128 v[12:15], v124 offset:20480
	ds_read_b64 v[16:17], v124 offset:21504
	v_exp_f32_e32 v68, v68
	v_exp_f32_e32 v69, v69
	v_exp_f32_e32 v70, v70
	v_exp_f32_e32 v71, v71
	v_pk_add_f32 v[120:121], v[120:121], v[68:69]
	v_pk_add_f32 v[122:123], v[122:123], v[70:71]
	v_mfma_f32_32x32x64_f8f6f4 v[80:95], v[18:23], v[114:119], v[80:95] cbsz:2 blgp:2
	ds_read_b128 v[18:21], v124 offset:22528
	ds_read_b64 v[22:23], v124 offset:23552
	v_exp_f32_e32 v72, v72
	v_exp_f32_e32 v73, v73
	v_exp_f32_e32 v74, v74
	v_exp_f32_e32 v75, v75
	v_pk_add_f32 v[120:121], v[120:121], v[72:73]
	v_pk_add_f32 v[122:123], v[122:123], v[74:75]
	s_waitcnt lgkmcnt(8)
	v_mfma_f32_32x32x64_f8f6f4 v[48:63], v[24:29], v[96:101], 0 cbsz:2 blgp:2
	ds_read_b128 v[24:27], v124 offset:24576
	ds_read_b64 v[28:29], v124 offset:25600
	v_exp_f32_e32 v76, v76
	v_exp_f32_e32 v77, v77
	v_exp_f32_e32 v78, v78
	v_exp_f32_e32 v79, v79
	v_pk_add_f32 v[120:121], v[120:121], v[76:77]
	v_pk_add_f32 v[122:123], v[122:123], v[78:79]
	s_cmp_lg_u32 s8, 10
	s_cbranch_scc1 .Lmk_nosplit
	v_add_f32_e32 v127, v120, v121
	v_add_f32_e32 v125, v122, v123
	v_mov_b32_e32 v120, 0
	v_mov_b32_e32 v121, 0
	v_mov_b32_e32 v122, 0
	v_mov_b32_e32 v123, 0
	v_add_f32_e32 v127, v127, v125
